# xattn: LDS fragment reads of the row-max and PV loops issued up front (both layers)
# speedup vs baseline: 1.0047x; 1.0047x over previous
.LBB0_861:
	v_add_u32_e32 v19, s2, v218
	s_nop 1
	ds_read_b128 v[2:5], v19
	ds_read_b128 v[28:31], v19 offset:32
	ds_read_b128 v[32:35], v19 offset:64
	ds_read_b128 v[36:39], v19 offset:96
	ds_read_b128 v[102:105], v19 offset:128
	ds_read_b128 v[110:113], v19 offset:160
	ds_read_b128 v[114:117], v19 offset:192
	ds_read_b128 v[118:121], v19 offset:224
	ds_read_b128 v[122:125], v19 offset:256
	ds_read_b128 v[126:129], v19 offset:288
	ds_read_b128 v[130:133], v19 offset:320
	ds_read_b128 v[134:137], v19 offset:352
	ds_read_b128 v[20:23], v19 offset:384
	ds_read_b128 v[24:27], v19 offset:416
	s_addk_i32 s2, 0x4200
	s_cmp_lg_u32 s2, 0x21000
	s_waitcnt lgkmcnt(13)
	v_mfma_f32_32x32x16_bf16 v[2:17], v[2:5], v[106:109], 0
	s_waitcnt lgkmcnt(12)
	v_mfma_f32_32x32x16_bf16 v[2:17], v[28:31], v[98:101], v[2:17]
	ds_read_b128 v[28:31], v19 offset:448
	s_waitcnt lgkmcnt(12)
	v_mfma_f32_32x32x16_bf16 v[2:17], v[32:35], v[94:97], v[2:17]
	ds_read_b128 v[32:35], v19 offset:480
	s_waitcnt lgkmcnt(12)
	v_mfma_f32_32x32x16_bf16 v[2:17], v[36:39], v[90:93], v[2:17]
	s_waitcnt lgkmcnt(11)
	v_mfma_f32_32x32x16_bf16 v[2:17], v[102:105], v[86:89], v[2:17]
	s_waitcnt lgkmcnt(10)
	v_mfma_f32_32x32x16_bf16 v[2:17], v[110:113], v[82:85], v[2:17]
	s_waitcnt lgkmcnt(9)
	v_mfma_f32_32x32x16_bf16 v[2:17], v[114:117], v[78:81], v[2:17]
	s_waitcnt lgkmcnt(8)
	v_mfma_f32_32x32x16_bf16 v[2:17], v[118:121], v[74:77], v[2:17]
	s_waitcnt lgkmcnt(7)
	v_mfma_f32_32x32x16_bf16 v[2:17], v[122:125], v[70:73], v[2:17]
	s_waitcnt lgkmcnt(6)
	v_mfma_f32_32x32x16_bf16 v[2:17], v[126:129], v[66:69], v[2:17]
	s_waitcnt lgkmcnt(5)
	v_mfma_f32_32x32x16_bf16 v[2:17], v[130:133], v[62:65], v[2:17]
	s_waitcnt lgkmcnt(4)
	v_mfma_f32_32x32x16_bf16 v[2:17], v[134:137], v[58:61], v[2:17]
	s_waitcnt lgkmcnt(3)
	v_mfma_f32_32x32x16_bf16 v[2:17], v[20:23], v[54:57], v[2:17]
	s_waitcnt lgkmcnt(2)
	v_mfma_f32_32x32x16_bf16 v[2:17], v[24:27], v[50:53], v[2:17]
	s_waitcnt lgkmcnt(1)
	v_mfma_f32_32x32x16_bf16 v[2:17], v[28:31], v[46:49], v[2:17]
	s_waitcnt lgkmcnt(0)
	v_mfma_f32_32x32x16_bf16 v[2:17], v[32:35], v[42:45], v[2:17]
	s_nop 11
	v_max3_f32 v2, v18, v2, v3
	v_max3_f32 v2, v2, v4, v5
	v_max3_f32 v2, v2, v6, v7
	v_max3_f32 v2, v2, v8, v9
	v_max3_f32 v2, v2, v10, v11
	v_max3_f32 v2, v2, v12, v13
	v_max3_f32 v2, v2, v14, v15
	v_max3_f32 v18, v2, v16, v17
	s_cbranch_scc1 .LBB0_861
	ds_read_b128 v[2:5], v166
	ds_read_b128 v[20:23], v166 offset:32
	ds_bpermute_b32 v19, v139, v18
	v_max_f32_e32 v18, v18, v18
	s_lshl_b32 s6, s14, 1
	s_waitcnt lgkmcnt(2)
	v_mfma_f32_32x32x16_bf16 v[2:17], v[2:5], v[106:109], 0
	s_and_b32 s2, s10, 0x1f00
	s_waitcnt lgkmcnt(0)
	v_max_f32_e32 v19, v19, v19
	v_max_f32_e32 v142, v18, v19
	s_and_b32 s6, s6, 0x600
	s_add_u32 s6, s12, s6
	s_addc_u32 s7, s13, 0
	v_mfma_f32_32x32x16_bf16 v[2:17], v[20:23], v[98:101], v[2:17]
	ds_read_b128 v[20:23], v166 offset:64
	ds_read_b128 v[24:27], v166 offset:96
	s_waitcnt lgkmcnt(1)
	v_mfma_f32_32x32x16_bf16 v[2:17], v[20:23], v[94:97], v[2:17]
	s_waitcnt lgkmcnt(0)
	v_mfma_f32_32x32x16_bf16 v[2:17], v[24:27], v[90:93], v[2:17]
	ds_read_b128 v[20:23], v166 offset:128
	ds_read_b128 v[24:27], v166 offset:160
	s_waitcnt lgkmcnt(1)
	v_mfma_f32_32x32x16_bf16 v[2:17], v[20:23], v[86:89], v[2:17]
	s_waitcnt lgkmcnt(0)
	v_mfma_f32_32x32x16_bf16 v[2:17], v[24:27], v[82:85], v[2:17]
	ds_read_b128 v[20:23], v166 offset:192
	ds_read_b128 v[24:27], v166 offset:224
	s_waitcnt lgkmcnt(1)
	v_mfma_f32_32x32x16_bf16 v[2:17], v[20:23], v[78:81], v[2:17]
	s_waitcnt lgkmcnt(0)
	v_mfma_f32_32x32x16_bf16 v[2:17], v[24:27], v[74:77], v[2:17]
	ds_read_b128 v[20:23], v166 offset:256
	ds_read_b128 v[24:27], v166 offset:288
	s_waitcnt lgkmcnt(1)
	v_mfma_f32_32x32x16_bf16 v[2:17], v[20:23], v[70:73], v[2:17]
	s_waitcnt lgkmcnt(0)
	v_mfma_f32_32x32x16_bf16 v[2:17], v[24:27], v[66:69], v[2:17]
	ds_read_b128 v[20:23], v166 offset:320
	ds_read_b128 v[24:27], v166 offset:352
	s_waitcnt lgkmcnt(1)
	v_mfma_f32_32x32x16_bf16 v[2:17], v[20:23], v[62:65], v[2:17]
	s_waitcnt lgkmcnt(0)
	v_mfma_f32_32x32x16_bf16 v[2:17], v[24:27], v[58:61], v[2:17]
	ds_read_b128 v[20:23], v166 offset:384
	ds_read_b128 v[24:27], v166 offset:416
	s_waitcnt lgkmcnt(1)
	v_mfma_f32_32x32x16_bf16 v[2:17], v[20:23], v[54:57], v[2:17]
	ds_read_b128 v[20:23], v166 offset:448
	s_waitcnt lgkmcnt(1)
	v_mfma_f32_32x32x16_bf16 v[2:17], v[24:27], v[50:53], v[2:17]
	ds_read_b128 v[24:27], v166 offset:480
	s_waitcnt lgkmcnt(1)
	v_mfma_f32_32x32x16_bf16 v[2:17], v[20:23], v[46:49], v[2:17]
	s_waitcnt lgkmcnt(0)
	v_mfma_f32_32x32x16_bf16 v[2:17], v[24:27], v[42:45], v[2:17]
	s_nop 11
	v_sub_f32_e32 v2, v2, v142
	v_sub_f32_e32 v3, v3, v142
	v_mul_f32_e32 v2, 0x3db8aa3b, v2
	v_mul_f32_e32 v3, 0x3db8aa3b, v3
	v_sub_f32_e32 v4, v4, v142
	v_exp_f32_e32 v2, v2
	v_exp_f32_e32 v3, v3
	v_sub_f32_e32 v5, v5, v142
	v_mul_f32_e32 v4, 0x3db8aa3b, v4
	v_sub_f32_e32 v6, v6, v142
	v_mul_f32_e32 v5, 0x3db8aa3b, v5
	v_exp_f32_e32 v4, v4
	v_sub_f32_e32 v7, v7, v142
	v_mul_f32_e32 v6, 0x3db8aa3b, v6
	v_exp_f32_e32 v5, v5
	v_sub_f32_e32 v8, v8, v142
	v_mul_f32_e32 v7, 0x3db8aa3b, v7
	v_exp_f32_e32 v6, v6
	v_cvt_pk_bf16_f32 v18, v2, v3
	v_add_f32_e32 v2, 0, v2
	v_sub_f32_e32 v9, v9, v142
	v_mul_f32_e32 v8, 0x3db8aa3b, v8
	v_exp_f32_e32 v7, v7
	v_add_f32_e32 v2, v3, v2
	v_sub_f32_e32 v10, v10, v142
	v_mul_f32_e32 v9, 0x3db8aa3b, v9
	v_exp_f32_e32 v8, v8
	v_add_f32_e32 v2, v4, v2
	v_sub_f32_e32 v11, v11, v142
	v_mul_f32_e32 v10, 0x3db8aa3b, v10
	v_exp_f32_e32 v9, v9
	v_add_f32_e32 v2, v5, v2
	v_sub_f32_e32 v12, v12, v142
	v_mul_f32_e32 v11, 0x3db8aa3b, v11
	v_exp_f32_e32 v10, v10
	v_add_f32_e32 v2, v6, v2
	v_sub_f32_e32 v13, v13, v142
	v_mul_f32_e32 v12, 0x3db8aa3b, v12
	v_exp_f32_e32 v11, v11
	v_add_f32_e32 v2, v7, v2
	v_sub_f32_e32 v14, v14, v142
	v_mul_f32_e32 v13, 0x3db8aa3b, v13
	v_exp_f32_e32 v12, v12
	v_add_f32_e32 v2, v8, v2
	v_sub_f32_e32 v15, v15, v142
	v_mul_f32_e32 v14, 0x3db8aa3b, v14
	v_exp_f32_e32 v13, v13
	v_add_f32_e32 v2, v9, v2
	v_sub_f32_e32 v16, v16, v142
	v_mul_f32_e32 v15, 0x3db8aa3b, v15
	v_exp_f32_e32 v14, v14
	v_add_f32_e32 v2, v10, v2
	v_sub_f32_e32 v17, v17, v142
	v_mul_f32_e32 v16, 0x3db8aa3b, v16
	v_exp_f32_e32 v15, v15
	v_add_f32_e32 v2, v11, v2
	v_mul_f32_e32 v17, 0x3db8aa3b, v17
	v_exp_f32_e32 v16, v16
	v_add_f32_e32 v2, v12, v2
	v_exp_f32_e32 v17, v17
	v_add_f32_e32 v2, v13, v2
	v_add_f32_e32 v2, v14, v2
	v_add_f32_e32 v2, v15, v2
	v_add_f32_e32 v2, v16, v2
	v_cvt_pk_bf16_f32 v19, v4, v5
	v_cvt_pk_bf16_f32 v20, v6, v7
	v_cvt_pk_bf16_f32 v21, v8, v9
	v_cvt_pk_bf16_f32 v22, v10, v11
	v_cvt_pk_bf16_f32 v23, v12, v13
	v_cvt_pk_bf16_f32 v24, v14, v15
	v_cvt_pk_bf16_f32 v25, v16, v17
	v_add_f32_e32 v34, v17, v2
	ds_read_b128 v[2:5], v166 offset:16896
	ds_read_b128 v[26:29], v166 offset:16928
	s_waitcnt lgkmcnt(1)
	v_mfma_f32_32x32x16_bf16 v[2:17], v[2:5], v[106:109], 0
	s_waitcnt lgkmcnt(0)
	v_mfma_f32_32x32x16_bf16 v[2:17], v[26:29], v[98:101], v[2:17]
	ds_read_b128 v[26:29], v166 offset:16960
	ds_read_b128 v[30:33], v166 offset:16992
	s_waitcnt lgkmcnt(1)
	v_mfma_f32_32x32x16_bf16 v[2:17], v[26:29], v[94:97], v[2:17]
	s_waitcnt lgkmcnt(0)
	v_mfma_f32_32x32x16_bf16 v[2:17], v[30:33], v[90:93], v[2:17]
	ds_read_b128 v[26:29], v166 offset:17024
	ds_read_b128 v[30:33], v166 offset:17056
	s_waitcnt lgkmcnt(1)
	v_mfma_f32_32x32x16_bf16 v[2:17], v[26:29], v[86:89], v[2:17]
	s_waitcnt lgkmcnt(0)
	v_mfma_f32_32x32x16_bf16 v[2:17], v[30:33], v[82:85], v[2:17]
	ds_read_b128 v[26:29], v166 offset:17088
	ds_read_b128 v[30:33], v166 offset:17120
	s_waitcnt lgkmcnt(1)
	v_mfma_f32_32x32x16_bf16 v[2:17], v[26:29], v[78:81], v[2:17]
	s_waitcnt lgkmcnt(0)
	v_mfma_f32_32x32x16_bf16 v[2:17], v[30:33], v[74:77], v[2:17]
	ds_read_b128 v[26:29], v166 offset:17152
	ds_read_b128 v[30:33], v166 offset:17184
	s_waitcnt lgkmcnt(1)
	v_mfma_f32_32x32x16_bf16 v[2:17], v[26:29], v[70:73], v[2:17]
	s_waitcnt lgkmcnt(0)
	v_mfma_f32_32x32x16_bf16 v[2:17], v[30:33], v[66:69], v[2:17]
	ds_read_b128 v[26:29], v166 offset:17216
	ds_read_b128 v[30:33], v166 offset:17248
	s_waitcnt lgkmcnt(1)
	v_mfma_f32_32x32x16_bf16 v[2:17], v[26:29], v[62:65], v[2:17]
	s_waitcnt lgkmcnt(0)
	v_mfma_f32_32x32x16_bf16 v[2:17], v[30:33], v[58:61], v[2:17]
	ds_read_b128 v[26:29], v166 offset:17280
	ds_read_b128 v[30:33], v166 offset:17312
	s_waitcnt lgkmcnt(1)
	v_mfma_f32_32x32x16_bf16 v[2:17], v[26:29], v[54:57], v[2:17]
	s_waitcnt lgkmcnt(0)
	v_mfma_f32_32x32x16_bf16 v[2:17], v[30:33], v[50:53], v[2:17]
	ds_read_b128 v[26:29], v166 offset:17344
	ds_read_b128 v[30:33], v166 offset:17376
	s_waitcnt lgkmcnt(1)
	v_mfma_f32_32x32x16_bf16 v[2:17], v[26:29], v[46:49], v[2:17]
	s_waitcnt lgkmcnt(0)
	v_mfma_f32_32x32x16_bf16 v[2:17], v[30:33], v[42:45], v[2:17]
	s_nop 11
	v_sub_f32_e32 v2, v2, v142
	v_sub_f32_e32 v3, v3, v142
	v_mul_f32_e32 v2, 0x3db8aa3b, v2
	v_mul_f32_e32 v3, 0x3db8aa3b, v3
	v_sub_f32_e32 v4, v4, v142
	v_exp_f32_e32 v2, v2
	v_exp_f32_e32 v3, v3
	v_sub_f32_e32 v5, v5, v142
	v_mul_f32_e32 v4, 0x3db8aa3b, v4
	v_sub_f32_e32 v6, v6, v142
	v_mul_f32_e32 v5, 0x3db8aa3b, v5
	v_exp_f32_e32 v4, v4
	v_sub_f32_e32 v7, v7, v142
	v_mul_f32_e32 v6, 0x3db8aa3b, v6
	v_exp_f32_e32 v5, v5
	v_sub_f32_e32 v8, v8, v142
	v_mul_f32_e32 v7, 0x3db8aa3b, v7
	v_exp_f32_e32 v6, v6
	v_cvt_pk_bf16_f32 v26, v2, v3
	v_add_f32_e32 v2, v34, v2
	v_sub_f32_e32 v9, v9, v142
	v_mul_f32_e32 v8, 0x3db8aa3b, v8
	v_exp_f32_e32 v7, v7
	v_add_f32_e32 v2, v3, v2
	v_sub_f32_e32 v10, v10, v142
	v_mul_f32_e32 v9, 0x3db8aa3b, v9
	v_exp_f32_e32 v8, v8
	v_add_f32_e32 v2, v4, v2
	v_sub_f32_e32 v11, v11, v142
	v_mul_f32_e32 v10, 0x3db8aa3b, v10
	v_exp_f32_e32 v9, v9
	v_add_f32_e32 v2, v5, v2
	v_sub_f32_e32 v12, v12, v142
	v_mul_f32_e32 v11, 0x3db8aa3b, v11
	v_exp_f32_e32 v10, v10
	v_add_f32_e32 v2, v6, v2
	v_sub_f32_e32 v13, v13, v142
	v_mul_f32_e32 v12, 0x3db8aa3b, v12
	v_exp_f32_e32 v11, v11
	v_add_f32_e32 v2, v7, v2
	v_sub_f32_e32 v14, v14, v142
	v_mul_f32_e32 v13, 0x3db8aa3b, v13
	v_exp_f32_e32 v12, v12
	v_add_f32_e32 v2, v8, v2
	v_sub_f32_e32 v15, v15, v142
	v_mul_f32_e32 v14, 0x3db8aa3b, v14
	v_exp_f32_e32 v13, v13
	v_add_f32_e32 v2, v9, v2
	v_sub_f32_e32 v16, v16, v142
	v_mul_f32_e32 v15, 0x3db8aa3b, v15
	v_exp_f32_e32 v14, v14
	v_add_f32_e32 v2, v10, v2
	v_sub_f32_e32 v17, v17, v142
	v_mul_f32_e32 v16, 0x3db8aa3b, v16
	v_exp_f32_e32 v15, v15
	v_add_f32_e32 v2, v11, v2
	v_mul_f32_e32 v17, 0x3db8aa3b, v17
	v_exp_f32_e32 v16, v16
	v_add_f32_e32 v2, v12, v2
	v_exp_f32_e32 v17, v17
	v_add_f32_e32 v2, v13, v2
	v_add_f32_e32 v2, v14, v2
	v_add_f32_e32 v2, v15, v2
	v_add_f32_e32 v2, v16, v2
	v_cvt_pk_bf16_f32 v27, v4, v5
	v_cvt_pk_bf16_f32 v28, v6, v7
	v_cvt_pk_bf16_f32 v29, v8, v9
	v_cvt_pk_bf16_f32 v30, v10, v11
	v_cvt_pk_bf16_f32 v31, v12, v13
	v_cvt_pk_bf16_f32 v32, v14, v15
	v_cvt_pk_bf16_f32 v33, v16, v17
	v_add_f32_e32 v102, v17, v2
	ds_read_b128 v[2:5], v166 offset:33792
	ds_read_b128 v[34:37], v166 offset:33824
	s_waitcnt lgkmcnt(1)
	v_mfma_f32_32x32x16_bf16 v[2:17], v[2:5], v[106:109], 0
	s_waitcnt lgkmcnt(0)
	v_mfma_f32_32x32x16_bf16 v[2:17], v[34:37], v[98:101], v[2:17]
	ds_read_b128 v[34:37], v166 offset:33856
	ds_read_b128 v[38:41], v166 offset:33888
	s_waitcnt lgkmcnt(1)
	v_mfma_f32_32x32x16_bf16 v[2:17], v[34:37], v[94:97], v[2:17]
	s_waitcnt lgkmcnt(0)
	v_mfma_f32_32x32x16_bf16 v[2:17], v[38:41], v[90:93], v[2:17]
	ds_read_b128 v[34:37], v166 offset:33920
	ds_read_b128 v[38:41], v166 offset:33952
	s_waitcnt lgkmcnt(1)
	v_mfma_f32_32x32x16_bf16 v[2:17], v[34:37], v[86:89], v[2:17]
	s_waitcnt lgkmcnt(0)
	v_mfma_f32_32x32x16_bf16 v[2:17], v[38:41], v[82:85], v[2:17]
	ds_read_b128 v[34:37], v166 offset:33984
	ds_read_b128 v[38:41], v166 offset:34016
	s_waitcnt lgkmcnt(1)
	v_mfma_f32_32x32x16_bf16 v[2:17], v[34:37], v[78:81], v[2:17]
	s_waitcnt lgkmcnt(0)
	v_mfma_f32_32x32x16_bf16 v[2:17], v[38:41], v[74:77], v[2:17]
	ds_read_b128 v[34:37], v166 offset:34048
	ds_read_b128 v[38:41], v166 offset:34080
	s_waitcnt lgkmcnt(1)
	v_mfma_f32_32x32x16_bf16 v[2:17], v[34:37], v[70:73], v[2:17]
	s_waitcnt lgkmcnt(0)
	v_mfma_f32_32x32x16_bf16 v[2:17], v[38:41], v[66:69], v[2:17]
	ds_read_b128 v[34:37], v166 offset:34112
	ds_read_b128 v[38:41], v166 offset:34144
	s_waitcnt lgkmcnt(1)
	v_mfma_f32_32x32x16_bf16 v[2:17], v[34:37], v[62:65], v[2:17]
	s_waitcnt lgkmcnt(0)
	v_mfma_f32_32x32x16_bf16 v[2:17], v[38:41], v[58:61], v[2:17]
	ds_read_b128 v[34:37], v166 offset:34176
	ds_read_b128 v[38:41], v166 offset:34208
	s_waitcnt lgkmcnt(1)
	v_mfma_f32_32x32x16_bf16 v[2:17], v[34:37], v[54:57], v[2:17]
	s_waitcnt lgkmcnt(0)
	v_mfma_f32_32x32x16_bf16 v[2:17], v[38:41], v[50:53], v[2:17]
	ds_read_b128 v[34:37], v166 offset:34240
	ds_read_b128 v[38:41], v166 offset:34272
	s_waitcnt lgkmcnt(1)
	v_mfma_f32_32x32x16_bf16 v[2:17], v[34:37], v[46:49], v[2:17]
	s_waitcnt lgkmcnt(0)
	v_mfma_f32_32x32x16_bf16 v[2:17], v[38:41], v[42:45], v[2:17]
	s_nop 11
	v_sub_f32_e32 v2, v2, v142
	v_sub_f32_e32 v3, v3, v142
	v_mul_f32_e32 v2, 0x3db8aa3b, v2
	v_mul_f32_e32 v3, 0x3db8aa3b, v3
	v_sub_f32_e32 v4, v4, v142
	v_exp_f32_e32 v2, v2
	v_exp_f32_e32 v3, v3
	v_sub_f32_e32 v5, v5, v142
	v_mul_f32_e32 v4, 0x3db8aa3b, v4
	v_sub_f32_e32 v6, v6, v142
	v_mul_f32_e32 v5, 0x3db8aa3b, v5
	v_exp_f32_e32 v4, v4
	v_sub_f32_e32 v7, v7, v142
	v_mul_f32_e32 v6, 0x3db8aa3b, v6
	v_exp_f32_e32 v5, v5
	v_sub_f32_e32 v8, v8, v142
	v_mul_f32_e32 v7, 0x3db8aa3b, v7
	v_exp_f32_e32 v6, v6
	v_cvt_pk_bf16_f32 v34, v2, v3
	v_add_f32_e32 v2, v102, v2
	v_sub_f32_e32 v9, v9, v142
	v_mul_f32_e32 v8, 0x3db8aa3b, v8
	v_exp_f32_e32 v7, v7
	v_add_f32_e32 v2, v3, v2
	v_sub_f32_e32 v10, v10, v142
	v_mul_f32_e32 v9, 0x3db8aa3b, v9
	v_exp_f32_e32 v8, v8
	v_add_f32_e32 v2, v4, v2
	v_sub_f32_e32 v11, v11, v142
	v_mul_f32_e32 v10, 0x3db8aa3b, v10
	v_exp_f32_e32 v9, v9
	v_add_f32_e32 v2, v5, v2
	v_sub_f32_e32 v12, v12, v142
	v_mul_f32_e32 v11, 0x3db8aa3b, v11
	v_exp_f32_e32 v10, v10
	v_add_f32_e32 v2, v6, v2
	v_sub_f32_e32 v13, v13, v142
	v_mul_f32_e32 v12, 0x3db8aa3b, v12
	v_exp_f32_e32 v11, v11
	v_add_f32_e32 v2, v7, v2
	v_sub_f32_e32 v14, v14, v142
	v_mul_f32_e32 v13, 0x3db8aa3b, v13
	v_exp_f32_e32 v12, v12
	v_add_f32_e32 v2, v8, v2
	v_sub_f32_e32 v15, v15, v142
	v_mul_f32_e32 v14, 0x3db8aa3b, v14
	v_exp_f32_e32 v13, v13
	v_add_f32_e32 v2, v9, v2
	v_sub_f32_e32 v16, v16, v142
	v_mul_f32_e32 v15, 0x3db8aa3b, v15
	v_exp_f32_e32 v14, v14
	v_add_f32_e32 v2, v10, v2
	v_sub_f32_e32 v17, v17, v142
	v_mul_f32_e32 v16, 0x3db8aa3b, v16
	v_exp_f32_e32 v15, v15
	v_add_f32_e32 v2, v11, v2
	v_mul_f32_e32 v17, 0x3db8aa3b, v17
	v_exp_f32_e32 v16, v16
	v_add_f32_e32 v2, v12, v2
	v_exp_f32_e32 v17, v17
	v_add_f32_e32 v2, v13, v2
	v_add_f32_e32 v2, v14, v2
	v_add_f32_e32 v2, v15, v2
	v_add_f32_e32 v2, v16, v2
	v_cvt_pk_bf16_f32 v35, v4, v5
	v_cvt_pk_bf16_f32 v36, v6, v7
	v_cvt_pk_bf16_f32 v37, v8, v9
	v_cvt_pk_bf16_f32 v38, v10, v11
	v_cvt_pk_bf16_f32 v39, v12, v13
	v_cvt_pk_bf16_f32 v40, v14, v15
	v_cvt_pk_bf16_f32 v41, v16, v17
	v_add_f32_e32 v114, v17, v2
	ds_read_b128 v[2:5], v166 offset:50688
	ds_read_b128 v[102:105], v166 offset:50720
	s_waitcnt lgkmcnt(1)
	v_mfma_f32_32x32x16_bf16 v[2:17], v[2:5], v[106:109], 0
	s_waitcnt lgkmcnt(0)
	v_mfma_f32_32x32x16_bf16 v[2:17], v[102:105], v[98:101], v[2:17]
	ds_read_b128 v[102:105], v166 offset:50752
	ds_read_b128 v[110:113], v166 offset:50784
	s_waitcnt lgkmcnt(1)
	v_mfma_f32_32x32x16_bf16 v[2:17], v[102:105], v[94:97], v[2:17]
	s_waitcnt lgkmcnt(0)
	v_mfma_f32_32x32x16_bf16 v[2:17], v[110:113], v[90:93], v[2:17]
	ds_read_b128 v[102:105], v166 offset:50816
	ds_read_b128 v[110:113], v166 offset:50848
	s_waitcnt lgkmcnt(1)
	v_mfma_f32_32x32x16_bf16 v[2:17], v[102:105], v[86:89], v[2:17]
	s_waitcnt lgkmcnt(0)
	v_mfma_f32_32x32x16_bf16 v[2:17], v[110:113], v[82:85], v[2:17]
	ds_read_b128 v[102:105], v166 offset:50880
	ds_read_b128 v[110:113], v166 offset:50912
	s_waitcnt lgkmcnt(1)
	v_mfma_f32_32x32x16_bf16 v[2:17], v[102:105], v[78:81], v[2:17]
	s_waitcnt lgkmcnt(0)
	v_mfma_f32_32x32x16_bf16 v[2:17], v[110:113], v[74:77], v[2:17]
	ds_read_b128 v[102:105], v166 offset:50944
	ds_read_b128 v[110:113], v166 offset:50976
	s_waitcnt lgkmcnt(1)
	v_mfma_f32_32x32x16_bf16 v[2:17], v[102:105], v[70:73], v[2:17]
	s_waitcnt lgkmcnt(0)
	v_mfma_f32_32x32x16_bf16 v[2:17], v[110:113], v[66:69], v[2:17]
	ds_read_b128 v[102:105], v166 offset:51008
	ds_read_b128 v[110:113], v166 offset:51040
	s_waitcnt lgkmcnt(1)
	v_mfma_f32_32x32x16_bf16 v[2:17], v[102:105], v[62:65], v[2:17]
	s_waitcnt lgkmcnt(0)
	v_mfma_f32_32x32x16_bf16 v[2:17], v[110:113], v[58:61], v[2:17]
	ds_read_b128 v[102:105], v166 offset:51072
	ds_read_b128 v[110:113], v166 offset:51104
	s_waitcnt lgkmcnt(1)
	v_mfma_f32_32x32x16_bf16 v[2:17], v[102:105], v[54:57], v[2:17]
	s_waitcnt lgkmcnt(0)
	v_mfma_f32_32x32x16_bf16 v[2:17], v[110:113], v[50:53], v[2:17]
	ds_read_b128 v[102:105], v166 offset:51136
	ds_read_b128 v[110:113], v166 offset:51168
	s_waitcnt lgkmcnt(1)
	v_mfma_f32_32x32x16_bf16 v[2:17], v[102:105], v[46:49], v[2:17]
	s_waitcnt lgkmcnt(0)
	v_mfma_f32_32x32x16_bf16 v[2:17], v[110:113], v[42:45], v[2:17]
	s_nop 11
	v_sub_f32_e32 v2, v2, v142
	v_sub_f32_e32 v3, v3, v142
	v_mul_f32_e32 v2, 0x3db8aa3b, v2
	v_mul_f32_e32 v3, 0x3db8aa3b, v3
	v_sub_f32_e32 v4, v4, v142
	v_exp_f32_e32 v2, v2
	v_exp_f32_e32 v3, v3
	v_sub_f32_e32 v5, v5, v142
	v_mul_f32_e32 v4, 0x3db8aa3b, v4
	v_sub_f32_e32 v6, v6, v142
	v_mul_f32_e32 v5, 0x3db8aa3b, v5
	v_exp_f32_e32 v4, v4
	v_sub_f32_e32 v7, v7, v142
	v_mul_f32_e32 v6, 0x3db8aa3b, v6
	v_exp_f32_e32 v5, v5
	v_sub_f32_e32 v8, v8, v142
	v_mul_f32_e32 v7, 0x3db8aa3b, v7
	v_exp_f32_e32 v6, v6
	v_cvt_pk_bf16_f32 v102, v2, v3
	v_add_f32_e32 v2, v114, v2
	v_sub_f32_e32 v9, v9, v142
	v_mul_f32_e32 v8, 0x3db8aa3b, v8
	v_exp_f32_e32 v7, v7
	v_add_f32_e32 v2, v3, v2
	v_sub_f32_e32 v10, v10, v142
	v_mul_f32_e32 v9, 0x3db8aa3b, v9
	v_exp_f32_e32 v8, v8
	v_add_f32_e32 v2, v4, v2
	v_sub_f32_e32 v11, v11, v142
	v_mul_f32_e32 v10, 0x3db8aa3b, v10
	v_exp_f32_e32 v9, v9
	v_add_f32_e32 v2, v5, v2
	v_sub_f32_e32 v12, v12, v142
	v_mul_f32_e32 v11, 0x3db8aa3b, v11
	v_exp_f32_e32 v10, v10
	v_add_f32_e32 v2, v6, v2
	v_sub_f32_e32 v13, v13, v142
	v_mul_f32_e32 v12, 0x3db8aa3b, v12
	v_exp_f32_e32 v11, v11
	v_add_f32_e32 v2, v7, v2
	v_sub_f32_e32 v14, v14, v142
	v_mul_f32_e32 v13, 0x3db8aa3b, v13
	v_exp_f32_e32 v12, v12
	v_add_f32_e32 v2, v8, v2
	v_sub_f32_e32 v15, v15, v142
	v_mul_f32_e32 v14, 0x3db8aa3b, v14
	v_exp_f32_e32 v13, v13
	v_add_f32_e32 v2, v9, v2
	v_sub_f32_e32 v16, v16, v142
	v_mul_f32_e32 v15, 0x3db8aa3b, v15
	v_exp_f32_e32 v14, v14
	v_add_f32_e32 v2, v10, v2
	v_sub_f32_e32 v17, v17, v142
	v_mul_f32_e32 v16, 0x3db8aa3b, v16
	v_exp_f32_e32 v15, v15
	v_add_f32_e32 v2, v11, v2
	v_mul_f32_e32 v17, 0x3db8aa3b, v17
	v_exp_f32_e32 v16, v16
	v_add_f32_e32 v2, v12, v2
	v_exp_f32_e32 v17, v17
	v_add_f32_e32 v2, v13, v2
	v_add_f32_e32 v2, v14, v2
	v_add_f32_e32 v2, v15, v2
	v_add_f32_e32 v2, v16, v2
	v_cvt_pk_bf16_f32 v103, v4, v5
	v_cvt_pk_bf16_f32 v104, v6, v7
	v_cvt_pk_bf16_f32 v105, v8, v9
	v_cvt_pk_bf16_f32 v110, v10, v11
	v_cvt_pk_bf16_f32 v111, v12, v13
	v_cvt_pk_bf16_f32 v112, v14, v15
	v_cvt_pk_bf16_f32 v113, v16, v17
	v_add_f32_e32 v122, v17, v2
	v_add_u32_e32 v2, 0x10800, v166
	ds_read_b128 v[2:5], v2
	v_add_u32_e32 v6, 0x10820, v166
	ds_read_b128 v[114:117], v6
	v_add_u32_e32 v118, 0x10840, v166
	s_waitcnt lgkmcnt(1)
	v_mfma_f32_32x32x16_bf16 v[2:17], v[2:5], v[106:109], 0
	s_waitcnt lgkmcnt(0)
	v_mfma_f32_32x32x16_bf16 v[2:17], v[114:117], v[98:101], v[2:17]
	ds_read_b128 v[114:117], v118
	v_add_u32_e32 v118, 0x10860, v166
	ds_read_b128 v[118:121], v118
	s_waitcnt lgkmcnt(1)
	v_mfma_f32_32x32x16_bf16 v[2:17], v[114:117], v[94:97], v[2:17]
	v_add_u32_e32 v114, 0x10880, v166
	ds_read_b128 v[114:117], v114
	s_waitcnt lgkmcnt(1)
	v_mfma_f32_32x32x16_bf16 v[2:17], v[118:121], v[90:93], v[2:17]
	v_add_u32_e32 v118, 0x108a0, v166
	ds_read_b128 v[118:121], v118
	s_waitcnt lgkmcnt(1)
	v_mfma_f32_32x32x16_bf16 v[2:17], v[114:117], v[86:89], v[2:17]
	v_add_u32_e32 v114, 0x108c0, v166
	ds_read_b128 v[114:117], v114
	s_waitcnt lgkmcnt(1)
	v_mfma_f32_32x32x16_bf16 v[2:17], v[118:121], v[82:85], v[2:17]
	v_add_u32_e32 v118, 0x108e0, v166
	ds_read_b128 v[118:121], v118
	s_waitcnt lgkmcnt(1)
	v_mfma_f32_32x32x16_bf16 v[2:17], v[114:117], v[78:81], v[2:17]
	v_add_u32_e32 v114, 0x10900, v166
	ds_read_b128 v[114:117], v114
	s_waitcnt lgkmcnt(1)
	v_mfma_f32_32x32x16_bf16 v[2:17], v[118:121], v[74:77], v[2:17]
	v_add_u32_e32 v118, 0x10920, v166
	ds_read_b128 v[118:121], v118
	s_waitcnt lgkmcnt(1)
	v_mfma_f32_32x32x16_bf16 v[2:17], v[114:117], v[70:73], v[2:17]
	v_add_u32_e32 v114, 0x10940, v166
	ds_read_b128 v[114:117], v114
	s_waitcnt lgkmcnt(1)
	v_mfma_f32_32x32x16_bf16 v[2:17], v[118:121], v[66:69], v[2:17]
	v_add_u32_e32 v118, 0x10960, v166
	ds_read_b128 v[118:121], v118
	s_waitcnt lgkmcnt(1)
	v_mfma_f32_32x32x16_bf16 v[2:17], v[114:117], v[62:65], v[2:17]
	v_add_u32_e32 v114, 0x10980, v166
	s_waitcnt lgkmcnt(0)
	v_mfma_f32_32x32x16_bf16 v[2:17], v[118:121], v[58:61], v[2:17]
	ds_read_b128 v[114:117], v114
	ds_read_b128 v[118:121], v167
	s_waitcnt lgkmcnt(1)
	v_mfma_f32_32x32x16_bf16 v[2:17], v[114:117], v[54:57], v[2:17]
	s_waitcnt lgkmcnt(0)
	v_mfma_f32_32x32x16_bf16 v[2:17], v[118:121], v[50:53], v[2:17]
	ds_read_b128 v[114:117], v168
	ds_read_b128 v[118:121], v169
	s_waitcnt lgkmcnt(1)
	v_mfma_f32_32x32x16_bf16 v[2:17], v[114:117], v[46:49], v[2:17]
	s_waitcnt lgkmcnt(0)
	v_mfma_f32_32x32x16_bf16 v[2:17], v[118:121], v[42:45], v[2:17]
	s_nop 11
	v_sub_f32_e32 v2, v2, v142
	v_sub_f32_e32 v3, v3, v142
	v_mul_f32_e32 v2, 0x3db8aa3b, v2
	v_mul_f32_e32 v3, 0x3db8aa3b, v3
	v_sub_f32_e32 v4, v4, v142
	v_exp_f32_e32 v2, v2
	v_exp_f32_e32 v3, v3
	v_sub_f32_e32 v5, v5, v142
	v_mul_f32_e32 v4, 0x3db8aa3b, v4
	v_sub_f32_e32 v6, v6, v142
	v_mul_f32_e32 v5, 0x3db8aa3b, v5
	v_exp_f32_e32 v4, v4
	v_sub_f32_e32 v7, v7, v142
	v_mul_f32_e32 v6, 0x3db8aa3b, v6
	v_exp_f32_e32 v5, v5
	v_sub_f32_e32 v8, v8, v142
	v_mul_f32_e32 v7, 0x3db8aa3b, v7
	v_exp_f32_e32 v6, v6
	v_cvt_pk_bf16_f32 v114, v2, v3
	v_add_f32_e32 v2, v122, v2
	v_sub_f32_e32 v9, v9, v142
	v_mul_f32_e32 v8, 0x3db8aa3b, v8
	v_exp_f32_e32 v7, v7
	v_add_f32_e32 v2, v3, v2
	v_sub_f32_e32 v10, v10, v142
	v_mul_f32_e32 v9, 0x3db8aa3b, v9
	v_exp_f32_e32 v8, v8
	v_add_f32_e32 v2, v4, v2
	v_sub_f32_e32 v11, v11, v142
	v_mul_f32_e32 v10, 0x3db8aa3b, v10
	v_exp_f32_e32 v9, v9
	v_add_f32_e32 v2, v5, v2
	v_sub_f32_e32 v12, v12, v142
	v_mul_f32_e32 v11, 0x3db8aa3b, v11
	v_exp_f32_e32 v10, v10
	v_add_f32_e32 v2, v6, v2
	v_sub_f32_e32 v13, v13, v142
	v_mul_f32_e32 v12, 0x3db8aa3b, v12
	v_exp_f32_e32 v11, v11
	v_add_f32_e32 v2, v7, v2
	v_sub_f32_e32 v14, v14, v142
	v_mul_f32_e32 v13, 0x3db8aa3b, v13
	v_exp_f32_e32 v12, v12
	v_add_f32_e32 v2, v8, v2
	v_sub_f32_e32 v15, v15, v142
	v_mul_f32_e32 v14, 0x3db8aa3b, v14
	v_exp_f32_e32 v13, v13
	v_add_f32_e32 v2, v9, v2
	v_sub_f32_e32 v16, v16, v142
	v_mul_f32_e32 v15, 0x3db8aa3b, v15
	v_exp_f32_e32 v14, v14
	v_add_f32_e32 v2, v10, v2
	v_sub_f32_e32 v17, v17, v142
	v_mul_f32_e32 v16, 0x3db8aa3b, v16
	v_exp_f32_e32 v15, v15
	v_add_f32_e32 v2, v11, v2
	v_mul_f32_e32 v17, 0x3db8aa3b, v17
	v_exp_f32_e32 v16, v16
	v_add_f32_e32 v2, v12, v2
	v_exp_f32_e32 v17, v17
	v_add_f32_e32 v2, v13, v2
	v_add_f32_e32 v2, v14, v2
	v_add_f32_e32 v2, v15, v2
	v_add_f32_e32 v2, v16, v2
	v_cvt_pk_bf16_f32 v115, v4, v5
	v_cvt_pk_bf16_f32 v116, v6, v7
	v_cvt_pk_bf16_f32 v117, v8, v9
	v_cvt_pk_bf16_f32 v118, v10, v11
	v_cvt_pk_bf16_f32 v119, v12, v13
	v_cvt_pk_bf16_f32 v120, v14, v15
	v_cvt_pk_bf16_f32 v121, v16, v17
	v_add_f32_e32 v130, v17, v2
	ds_read_b128 v[2:5], v170
	ds_read_b128 v[122:125], v171
	s_waitcnt lgkmcnt(1)
	v_mfma_f32_32x32x16_bf16 v[2:17], v[2:5], v[106:109], 0
	s_waitcnt lgkmcnt(0)
	v_mfma_f32_32x32x16_bf16 v[2:17], v[122:125], v[98:101], v[2:17]
	ds_read_b128 v[122:125], v172
	ds_read_b128 v[126:129], v173
	s_waitcnt lgkmcnt(1)
	v_mfma_f32_32x32x16_bf16 v[2:17], v[122:125], v[94:97], v[2:17]
	s_waitcnt lgkmcnt(0)
	v_mfma_f32_32x32x16_bf16 v[2:17], v[126:129], v[90:93], v[2:17]
	ds_read_b128 v[122:125], v174
	ds_read_b128 v[126:129], v175
	s_waitcnt lgkmcnt(1)
	v_mfma_f32_32x32x16_bf16 v[2:17], v[122:125], v[86:89], v[2:17]
	s_waitcnt lgkmcnt(0)
	v_mfma_f32_32x32x16_bf16 v[2:17], v[126:129], v[82:85], v[2:17]
	ds_read_b128 v[122:125], v176
	ds_read_b128 v[126:129], v177
	s_waitcnt lgkmcnt(1)
	v_mfma_f32_32x32x16_bf16 v[2:17], v[122:125], v[78:81], v[2:17]
	s_waitcnt lgkmcnt(0)
	v_mfma_f32_32x32x16_bf16 v[2:17], v[126:129], v[74:77], v[2:17]
	ds_read_b128 v[122:125], v178
	ds_read_b128 v[126:129], v179
	s_waitcnt lgkmcnt(1)
	v_mfma_f32_32x32x16_bf16 v[2:17], v[122:125], v[70:73], v[2:17]
	s_waitcnt lgkmcnt(0)
	v_mfma_f32_32x32x16_bf16 v[2:17], v[126:129], v[66:69], v[2:17]
	ds_read_b128 v[122:125], v180
	ds_read_b128 v[126:129], v181
	s_waitcnt lgkmcnt(1)
	v_mfma_f32_32x32x16_bf16 v[2:17], v[122:125], v[62:65], v[2:17]
	s_waitcnt lgkmcnt(0)
	v_mfma_f32_32x32x16_bf16 v[2:17], v[126:129], v[58:61], v[2:17]
	ds_read_b128 v[122:125], v182
	ds_read_b128 v[126:129], v183
	s_waitcnt lgkmcnt(1)
	v_mfma_f32_32x32x16_bf16 v[2:17], v[122:125], v[54:57], v[2:17]
	s_waitcnt lgkmcnt(0)
	v_mfma_f32_32x32x16_bf16 v[2:17], v[126:129], v[50:53], v[2:17]
	ds_read_b128 v[122:125], v184
	ds_read_b128 v[126:129], v185
	s_waitcnt lgkmcnt(1)
	v_mfma_f32_32x32x16_bf16 v[2:17], v[122:125], v[46:49], v[2:17]
	s_waitcnt lgkmcnt(0)
	v_mfma_f32_32x32x16_bf16 v[2:17], v[126:129], v[42:45], v[2:17]
	s_nop 11
	v_sub_f32_e32 v2, v2, v142
	v_sub_f32_e32 v3, v3, v142
	v_mul_f32_e32 v2, 0x3db8aa3b, v2
	v_mul_f32_e32 v3, 0x3db8aa3b, v3
	v_sub_f32_e32 v4, v4, v142
	v_exp_f32_e32 v2, v2
	v_exp_f32_e32 v3, v3
	v_sub_f32_e32 v5, v5, v142
	v_mul_f32_e32 v4, 0x3db8aa3b, v4
	v_sub_f32_e32 v6, v6, v142
	v_mul_f32_e32 v5, 0x3db8aa3b, v5
	v_exp_f32_e32 v4, v4
	v_sub_f32_e32 v7, v7, v142
	v_mul_f32_e32 v6, 0x3db8aa3b, v6
	v_exp_f32_e32 v5, v5
	v_sub_f32_e32 v8, v8, v142
	v_mul_f32_e32 v7, 0x3db8aa3b, v7
	v_exp_f32_e32 v6, v6
	v_cvt_pk_bf16_f32 v122, v2, v3
	v_add_f32_e32 v2, v130, v2
	v_sub_f32_e32 v9, v9, v142
	v_mul_f32_e32 v8, 0x3db8aa3b, v8
	v_exp_f32_e32 v7, v7
	v_add_f32_e32 v2, v3, v2
	v_sub_f32_e32 v10, v10, v142
	v_mul_f32_e32 v9, 0x3db8aa3b, v9
	v_exp_f32_e32 v8, v8
	v_add_f32_e32 v2, v4, v2
	v_sub_f32_e32 v11, v11, v142
	v_mul_f32_e32 v10, 0x3db8aa3b, v10
	v_exp_f32_e32 v9, v9
	v_add_f32_e32 v2, v5, v2
	v_sub_f32_e32 v12, v12, v142
	v_mul_f32_e32 v11, 0x3db8aa3b, v11
	v_exp_f32_e32 v10, v10
	v_add_f32_e32 v2, v6, v2
	v_sub_f32_e32 v13, v13, v142
	v_mul_f32_e32 v12, 0x3db8aa3b, v12
	v_exp_f32_e32 v11, v11
	v_add_f32_e32 v2, v7, v2
	v_sub_f32_e32 v14, v14, v142
	v_mul_f32_e32 v13, 0x3db8aa3b, v13
	v_exp_f32_e32 v12, v12
	v_add_f32_e32 v2, v8, v2
	v_sub_f32_e32 v15, v15, v142
	v_mul_f32_e32 v14, 0x3db8aa3b, v14
	v_exp_f32_e32 v13, v13
	v_add_f32_e32 v2, v9, v2
	v_sub_f32_e32 v16, v16, v142
	v_sub_f32_e32 v17, v17, v142
	v_mul_f32_e32 v15, 0x3db8aa3b, v15
	v_exp_f32_e32 v14, v14
	v_add_f32_e32 v2, v10, v2
	v_mul_f32_e32 v16, 0x3db8aa3b, v16
	v_mul_f32_e32 v17, 0x3db8aa3b, v17
	v_exp_f32_e32 v15, v15
	v_add_f32_e32 v2, v11, v2
	v_exp_f32_e32 v16, v16
	v_exp_f32_e32 v17, v17
	v_add_f32_e32 v2, v12, v2
	v_add_f32_e32 v2, v13, v2
	v_add_f32_e32 v2, v14, v2
	v_add_f32_e32 v2, v15, v2
	v_cvt_pk_bf16_f32 v123, v4, v5
	v_cvt_pk_bf16_f32 v124, v6, v7
	v_cvt_pk_bf16_f32 v125, v8, v9
	v_cvt_pk_bf16_f32 v126, v10, v11
	v_cvt_pk_bf16_f32 v127, v12, v13
	v_cvt_pk_bf16_f32 v128, v14, v15
	v_cvt_pk_bf16_f32 v129, v16, v17
	v_add_f32_e32 v2, v16, v2
	v_add_f32_e32 v149, v17, v2
	ds_read_b128 v[2:5], v186
	ds_read_b128 v[130:133], v187
	s_waitcnt lgkmcnt(1)
	v_mfma_f32_32x32x16_bf16 v[2:17], v[2:5], v[106:109], 0
	s_waitcnt lgkmcnt(0)
	v_mfma_f32_32x32x16_bf16 v[2:17], v[130:133], v[98:101], v[2:17]
	ds_read_b128 v[130:133], v188
	ds_read_b128 v[134:137], v189
	s_waitcnt lgkmcnt(1)
	v_mfma_f32_32x32x16_bf16 v[2:17], v[130:133], v[94:97], v[2:17]
	s_waitcnt lgkmcnt(0)
	v_mfma_f32_32x32x16_bf16 v[2:17], v[134:137], v[90:93], v[2:17]
	ds_read_b128 v[130:133], v190
	ds_read_b128 v[134:137], v191
	s_waitcnt lgkmcnt(1)
	v_mfma_f32_32x32x16_bf16 v[2:17], v[130:133], v[86:89], v[2:17]
	s_waitcnt lgkmcnt(0)
	v_mfma_f32_32x32x16_bf16 v[2:17], v[134:137], v[82:85], v[2:17]
	ds_read_b128 v[130:133], v192
	ds_read_b128 v[134:137], v193
	s_waitcnt lgkmcnt(1)
	v_mfma_f32_32x32x16_bf16 v[2:17], v[130:133], v[78:81], v[2:17]
	s_waitcnt lgkmcnt(0)
	v_mfma_f32_32x32x16_bf16 v[2:17], v[134:137], v[74:77], v[2:17]
	ds_read_b128 v[130:133], v194
	ds_read_b128 v[134:137], v195
	s_waitcnt lgkmcnt(1)
	v_mfma_f32_32x32x16_bf16 v[2:17], v[130:133], v[70:73], v[2:17]
	s_waitcnt lgkmcnt(0)
	v_mfma_f32_32x32x16_bf16 v[2:17], v[134:137], v[66:69], v[2:17]
	ds_read_b128 v[130:133], v196
	ds_read_b128 v[134:137], v197
	s_waitcnt lgkmcnt(1)
	v_mfma_f32_32x32x16_bf16 v[2:17], v[130:133], v[62:65], v[2:17]
	s_waitcnt lgkmcnt(0)
	v_mfma_f32_32x32x16_bf16 v[2:17], v[134:137], v[58:61], v[2:17]
	ds_read_b128 v[130:133], v198
	ds_read_b128 v[134:137], v199
	s_waitcnt lgkmcnt(1)
	v_mfma_f32_32x32x16_bf16 v[2:17], v[130:133], v[54:57], v[2:17]
	s_waitcnt lgkmcnt(0)
	v_mfma_f32_32x32x16_bf16 v[2:17], v[134:137], v[50:53], v[2:17]
	ds_read_b128 v[130:133], v200
	ds_read_b128 v[134:137], v201
	s_waitcnt lgkmcnt(1)
	v_mfma_f32_32x32x16_bf16 v[2:17], v[130:133], v[46:49], v[2:17]
	s_waitcnt lgkmcnt(0)
	v_mfma_f32_32x32x16_bf16 v[2:17], v[134:137], v[42:45], v[2:17]
	s_nop 11
	v_sub_f32_e32 v2, v2, v142
	v_sub_f32_e32 v3, v3, v142
	v_mul_f32_e32 v2, 0x3db8aa3b, v2
	v_mul_f32_e32 v3, 0x3db8aa3b, v3
	v_sub_f32_e32 v4, v4, v142
	v_exp_f32_e32 v2, v2
	v_exp_f32_e32 v3, v3
	v_sub_f32_e32 v5, v5, v142
	v_mul_f32_e32 v4, 0x3db8aa3b, v4
	v_sub_f32_e32 v6, v6, v142
	v_mul_f32_e32 v5, 0x3db8aa3b, v5
	v_exp_f32_e32 v4, v4
	v_sub_f32_e32 v7, v7, v142
	v_mul_f32_e32 v6, 0x3db8aa3b, v6
	v_exp_f32_e32 v5, v5
	v_sub_f32_e32 v8, v8, v142
	v_mul_f32_e32 v7, 0x3db8aa3b, v7
	v_exp_f32_e32 v6, v6
	v_cvt_pk_bf16_f32 v130, v2, v3
	v_add_f32_e32 v2, v149, v2
	v_sub_f32_e32 v9, v9, v142
	v_mul_f32_e32 v8, 0x3db8aa3b, v8
	v_exp_f32_e32 v7, v7
	v_add_f32_e32 v2, v3, v2
	v_sub_f32_e32 v10, v10, v142
	v_mul_f32_e32 v9, 0x3db8aa3b, v9
	v_exp_f32_e32 v8, v8
	v_add_f32_e32 v2, v4, v2
	v_sub_f32_e32 v11, v11, v142
	v_mul_f32_e32 v10, 0x3db8aa3b, v10
	v_exp_f32_e32 v9, v9
	v_add_f32_e32 v2, v5, v2
	v_sub_f32_e32 v12, v12, v142
	v_mul_f32_e32 v11, 0x3db8aa3b, v11
	v_exp_f32_e32 v10, v10
	v_add_f32_e32 v2, v6, v2
	v_sub_f32_e32 v13, v13, v142
	v_mul_f32_e32 v12, 0x3db8aa3b, v12
	v_exp_f32_e32 v11, v11
	v_add_f32_e32 v2, v7, v2
	v_sub_f32_e32 v14, v14, v142
	v_mul_f32_e32 v13, 0x3db8aa3b, v13
	v_exp_f32_e32 v12, v12
	v_add_f32_e32 v2, v8, v2
	v_sub_f32_e32 v15, v15, v142
	v_mul_f32_e32 v14, 0x3db8aa3b, v14
	v_exp_f32_e32 v13, v13
	v_add_f32_e32 v2, v9, v2
	v_sub_f32_e32 v16, v16, v142
	v_sub_f32_e32 v17, v17, v142
	v_mul_f32_e32 v15, 0x3db8aa3b, v15
	v_exp_f32_e32 v14, v14
	v_add_f32_e32 v2, v10, v2
	v_mul_f32_e32 v16, 0x3db8aa3b, v16
	v_mul_f32_e32 v17, 0x3db8aa3b, v17
	v_exp_f32_e32 v15, v15
	v_add_f32_e32 v2, v11, v2
	v_exp_f32_e32 v16, v16
	v_exp_f32_e32 v17, v17
	v_add_f32_e32 v2, v12, v2
	v_add_f32_e32 v2, v13, v2
	v_add_f32_e32 v2, v14, v2
	v_add_f32_e32 v2, v15, v2
	v_cvt_pk_bf16_f32 v131, v4, v5
	v_cvt_pk_bf16_f32 v132, v6, v7
	v_cvt_pk_bf16_f32 v133, v8, v9
	v_cvt_pk_bf16_f32 v134, v10, v11
	v_cvt_pk_bf16_f32 v135, v12, v13
	v_cvt_pk_bf16_f32 v136, v14, v15
	v_cvt_pk_bf16_f32 v137, v16, v17
	v_add_f32_e32 v2, v16, v2
	v_add_f32_e32 v149, v17, v2
	ds_read_b128 v[2:5], v202
	s_waitcnt lgkmcnt(0)
	v_mfma_f32_32x32x16_bf16 v[2:17], v[2:5], v[106:109], 0
	ds_read_b128 v[106:109], v203
	s_waitcnt lgkmcnt(0)
	v_mfma_f32_32x32x16_bf16 v[2:17], v[106:109], v[98:101], v[2:17]
	ds_read_b128 v[98:101], v204
	s_waitcnt lgkmcnt(0)
	v_mfma_f32_32x32x16_bf16 v[2:17], v[98:101], v[94:97], v[2:17]
	ds_read_b128 v[94:97], v205
	s_waitcnt lgkmcnt(0)
	v_mfma_f32_32x32x16_bf16 v[2:17], v[94:97], v[90:93], v[2:17]
	ds_read_b128 v[90:93], v206
	s_waitcnt lgkmcnt(0)
	v_mfma_f32_32x32x16_bf16 v[2:17], v[90:93], v[86:89], v[2:17]
	ds_read_b128 v[86:89], v207
	s_waitcnt lgkmcnt(0)
	v_mfma_f32_32x32x16_bf16 v[2:17], v[86:89], v[82:85], v[2:17]
	ds_read_b128 v[82:85], v208
	s_waitcnt lgkmcnt(0)
	v_mfma_f32_32x32x16_bf16 v[2:17], v[82:85], v[78:81], v[2:17]
	ds_read_b128 v[78:81], v209
	s_waitcnt lgkmcnt(0)
	v_mfma_f32_32x32x16_bf16 v[2:17], v[78:81], v[74:77], v[2:17]
	ds_read_b128 v[74:77], v210
	s_waitcnt lgkmcnt(0)
	v_mfma_f32_32x32x16_bf16 v[2:17], v[74:77], v[70:73], v[2:17]
	ds_read_b128 v[70:73], v211
	s_waitcnt lgkmcnt(0)
	v_mfma_f32_32x32x16_bf16 v[2:17], v[70:73], v[66:69], v[2:17]
	ds_read_b128 v[66:69], v212
	s_waitcnt lgkmcnt(0)
	v_mfma_f32_32x32x16_bf16 v[2:17], v[66:69], v[62:65], v[2:17]
	ds_read_b128 v[62:65], v213
	s_waitcnt lgkmcnt(0)
	v_mfma_f32_32x32x16_bf16 v[2:17], v[62:65], v[58:61], v[2:17]
	ds_read_b128 v[58:61], v214
	s_waitcnt lgkmcnt(0)
	v_mfma_f32_32x32x16_bf16 v[2:17], v[58:61], v[54:57], v[2:17]
	ds_read_b128 v[54:57], v215
	s_waitcnt lgkmcnt(0)
	v_mfma_f32_32x32x16_bf16 v[2:17], v[54:57], v[50:53], v[2:17]
	ds_read_b128 v[50:53], v216
	s_waitcnt lgkmcnt(0)
	v_mfma_f32_32x32x16_bf16 v[2:17], v[50:53], v[46:49], v[2:17]
	ds_read_b128 v[46:49], v217
	s_waitcnt lgkmcnt(0)
	v_mfma_f32_32x32x16_bf16 v[2:17], v[46:49], v[42:45], v[2:17]
	s_nop 11
	v_sub_f32_e32 v2, v2, v142
	v_sub_f32_e32 v3, v3, v142
	v_mul_f32_e32 v2, 0x3db8aa3b, v2
	v_mul_f32_e32 v3, 0x3db8aa3b, v3
	v_exp_f32_e32 v2, v2
	v_exp_f32_e32 v3, v3
	v_sub_f32_e32 v4, v4, v142
	v_mul_f32_e32 v4, 0x3db8aa3b, v4
	v_sub_f32_e32 v5, v5, v142
	v_exp_f32_e32 v4, v4
	v_mul_f32_e32 v5, 0x3db8aa3b, v5
	v_sub_f32_e32 v6, v6, v142
	v_exp_f32_e32 v5, v5
	v_mul_f32_e32 v6, 0x3db8aa3b, v6
	v_sub_f32_e32 v7, v7, v142
	v_exp_f32_e32 v6, v6
	v_mul_f32_e32 v7, 0x3db8aa3b, v7
	v_sub_f32_e32 v8, v8, v142
	v_cvt_pk_bf16_f32 v42, v2, v3
	v_add_f32_e32 v2, v149, v2
	v_exp_f32_e32 v7, v7
	v_mul_f32_e32 v8, 0x3db8aa3b, v8
	v_sub_f32_e32 v9, v9, v142
	v_add_f32_e32 v2, v3, v2
	v_exp_f32_e32 v8, v8
	v_mul_f32_e32 v9, 0x3db8aa3b, v9
	v_sub_f32_e32 v10, v10, v142
	v_add_f32_e32 v2, v4, v2
	v_exp_f32_e32 v9, v9
	v_mul_f32_e32 v10, 0x3db8aa3b, v10
	v_sub_f32_e32 v11, v11, v142
	v_add_f32_e32 v2, v5, v2
	v_exp_f32_e32 v10, v10
	v_mul_f32_e32 v11, 0x3db8aa3b, v11
	v_sub_f32_e32 v12, v12, v142
	v_add_f32_e32 v2, v6, v2
	v_exp_f32_e32 v11, v11
	v_mul_f32_e32 v12, 0x3db8aa3b, v12
	v_sub_f32_e32 v13, v13, v142
	v_add_f32_e32 v2, v7, v2
	v_exp_f32_e32 v12, v12
	v_mul_f32_e32 v13, 0x3db8aa3b, v13
	v_sub_f32_e32 v14, v14, v142
	v_add_f32_e32 v2, v8, v2
	v_exp_f32_e32 v13, v13
	v_mul_f32_e32 v14, 0x3db8aa3b, v14
	v_sub_f32_e32 v15, v15, v142
	v_add_f32_e32 v2, v9, v2
	v_exp_f32_e32 v14, v14
	v_mul_f32_e32 v15, 0x3db8aa3b, v15
	v_sub_f32_e32 v16, v16, v142
	v_sub_f32_e32 v17, v17, v142
	v_add_f32_e32 v2, v10, v2
	v_exp_f32_e32 v15, v15
	v_mul_f32_e32 v16, 0x3db8aa3b, v16
	v_mul_f32_e32 v17, 0x3db8aa3b, v17
	v_add_f32_e32 v2, v11, v2
	v_exp_f32_e32 v16, v16
	v_exp_f32_e32 v17, v17
	v_add_f32_e32 v2, v12, v2
	v_add_f32_e32 v2, v13, v2
	v_add_f32_e32 v2, v14, v2
	v_add_f32_e32 v2, v15, v2
	v_cvt_pk_bf16_f32 v43, v4, v5
	v_cvt_pk_bf16_f32 v44, v6, v7
	v_cvt_pk_bf16_f32 v45, v8, v9
	v_cvt_pk_bf16_f32 v46, v10, v11
	v_cvt_pk_bf16_f32 v47, v12, v13
	v_cvt_pk_bf16_f32 v48, v14, v15
	v_cvt_pk_bf16_f32 v49, v16, v17
	v_add_f32_e32 v2, v16, v2
	v_add_f32_e32 v98, v17, v2
	s_lshl_b32 s8, s8, 10
	s_or_b32 s8, s9, s8
	v_add_u32_e32 v2, s8, v150
	v_add_u32_e32 v4, s8, v151
	v_add_u32_e32 v10, s8, v152
	v_add_u32_e32 v12, s8, v153
	v_add_u32_e32 v50, s8, v154
	v_add_u32_e32 v52, s8, v155
	v_add_u32_e32 v58, s8, v156
	v_add_u32_e32 v60, s8, v157
	v_add_u32_e32 v66, s8, v158
	v_add_u32_e32 v68, s8, v159
	v_add_u32_e32 v74, s8, v160
	v_add_u32_e32 v76, s8, v161
	v_ashrrev_i32_e32 v3, 31, v2
	v_ashrrev_i32_e32 v5, 31, v4
	v_ashrrev_i32_e32 v11, 31, v10
	v_ashrrev_i32_e32 v13, 31, v12
	v_ashrrev_i32_e32 v51, 31, v50
	v_ashrrev_i32_e32 v53, 31, v52
	v_ashrrev_i32_e32 v59, 31, v58
	v_ashrrev_i32_e32 v61, 31, v60
	v_ashrrev_i32_e32 v67, 31, v66
	v_ashrrev_i32_e32 v69, 31, v68
	v_ashrrev_i32_e32 v75, 31, v74
	v_ashrrev_i32_e32 v77, 31, v76
	v_add_u32_e32 v82, s8, v162
	v_add_u32_e32 v84, s8, v163
	v_lshlrev_b64 v[2:3], 9, v[2:3]
	v_lshlrev_b64 v[4:5], 9, v[4:5]
	v_lshlrev_b64 v[10:11], 9, v[10:11]
	v_lshlrev_b64 v[12:13], 9, v[12:13]
	v_lshlrev_b64 v[50:51], 9, v[50:51]
	v_lshlrev_b64 v[52:53], 9, v[52:53]
	v_lshlrev_b64 v[58:59], 9, v[58:59]
	v_lshlrev_b64 v[60:61], 9, v[60:61]
	v_lshlrev_b64 v[66:67], 9, v[66:67]
	v_lshlrev_b64 v[68:69], 9, v[68:69]
	v_lshlrev_b64 v[74:75], 9, v[74:75]
	v_lshlrev_b64 v[76:77], 9, v[76:77]
	v_ashrrev_i32_e32 v83, 31, v82
	v_ashrrev_i32_e32 v85, 31, v84
	v_lshl_add_u64 v[2:3], v[146:147], 0, v[2:3]
	v_lshl_add_u64 v[6:7], v[146:147], 0, v[4:5]
	v_lshl_add_u64 v[10:11], v[146:147], 0, v[10:11]
	v_lshl_add_u64 v[14:15], v[146:147], 0, v[12:13]
	v_lshl_add_u64 v[50:51], v[146:147], 0, v[50:51]
	v_lshl_add_u64 v[54:55], v[146:147], 0, v[52:53]
	v_lshl_add_u64 v[58:59], v[146:147], 0, v[58:59]
	v_lshl_add_u64 v[62:63], v[146:147], 0, v[60:61]
	v_lshl_add_u64 v[66:67], v[146:147], 0, v[66:67]
	v_lshl_add_u64 v[70:71], v[146:147], 0, v[68:69]
	v_lshl_add_u64 v[74:75], v[146:147], 0, v[74:75]
	v_lshl_add_u64 v[78:79], v[146:147], 0, v[76:77]
	v_lshlrev_b64 v[82:83], 9, v[82:83]
	v_lshlrev_b64 v[84:85], 9, v[84:85]
	s_barrier
	global_load_dwordx4 v[2:5], v[2:3], off
	s_nop 0
	global_load_dwordx4 v[6:9], v[6:7], off
	s_nop 0
	global_load_dwordx4 v[10:13], v[10:11], off
	s_nop 0
	global_load_dwordx4 v[14:17], v[14:15], off
	s_nop 0
	global_load_dwordx4 v[50:53], v[50:51], off
	s_nop 0
	global_load_dwordx4 v[54:57], v[54:55], off
	s_nop 0
	global_load_dwordx4 v[58:61], v[58:59], off
	s_nop 0
	global_load_dwordx4 v[62:65], v[62:63], off
	s_nop 0
	global_load_dwordx4 v[66:69], v[66:67], off
	s_nop 0
	global_load_dwordx4 v[70:73], v[70:71], off
	s_nop 0
	global_load_dwordx4 v[74:77], v[74:75], off
	s_nop 0
	global_load_dwordx4 v[78:81], v[78:79], off
	v_lshl_add_u64 v[82:83], v[146:147], 0, v[82:83]
	v_lshl_add_u64 v[86:87], v[146:147], 0, v[84:85]
	global_load_dwordx4 v[82:85], v[82:83], off
	s_nop 0
	global_load_dwordx4 v[86:89], v[86:87], off
	v_add_u32_e32 v90, s8, v164
	v_add_u32_e32 v92, s8, v165
	v_ashrrev_i32_e32 v91, 31, v90
	v_ashrrev_i32_e32 v93, 31, v92
	v_lshlrev_b64 v[90:91], 9, v[90:91]
	v_lshlrev_b64 v[92:93], 9, v[92:93]
	v_lshl_add_u64 v[90:91], v[146:147], 0, v[90:91]
	v_lshl_add_u64 v[94:95], v[146:147], 0, v[92:93]
	global_load_dwordx4 v[90:93], v[90:91], off
	s_nop 0
	global_load_dwordx4 v[94:97], v[94:95], off
	ds_bpermute_b32 v99, v139, v98
	s_add_u32 s4, s4, s2
	s_addc_u32 s5, s5, 0
	s_mov_b32 s2, 0
	s_waitcnt vmcnt(15)
	ds_write2_b64 v236, v[2:3], v[4:5] offset1:1
	s_waitcnt vmcnt(14)
	ds_write2_b64 v237, v[6:7], v[8:9] offset1:1
	s_waitcnt vmcnt(13)
	ds_write2_b64 v238, v[10:11], v[12:13] offset1:1
	s_waitcnt vmcnt(12)
	ds_write2_b64 v239, v[14:15], v[16:17] offset1:1
	s_waitcnt vmcnt(11)
	ds_write2_b64 v240, v[50:51], v[52:53] offset1:1
	s_waitcnt vmcnt(10)
	ds_write2_b64 v241, v[54:55], v[56:57] offset1:1
	s_waitcnt vmcnt(9)
	ds_write2_b64 v242, v[58:59], v[60:61] offset1:1
	s_waitcnt vmcnt(8)
	ds_write2_b64 v243, v[62:63], v[64:65] offset1:1
	s_waitcnt vmcnt(7)
	ds_write2_b64 v244, v[66:67], v[68:69] offset1:1
	s_waitcnt vmcnt(6)
	ds_write2_b64 v245, v[70:71], v[72:73] offset1:1
	s_waitcnt vmcnt(5)
	ds_write2_b64 v246, v[74:75], v[76:77] offset1:1
	s_waitcnt vmcnt(4)
	ds_write2_b64 v247, v[78:79], v[80:81] offset1:1
	s_waitcnt vmcnt(3)
	ds_write2_b64 v248, v[82:83], v[84:85] offset1:1
	s_waitcnt lgkmcnt(13)
	v_add_f32_e32 v98, v98, v99
	v_div_scale_f32 v2, s[8:9], v98, v98, 1.0
	v_rcp_f32_e32 v3, v2
	s_waitcnt vmcnt(2)
	ds_write2_b64 v249, v[86:87], v[88:89] offset1:1
	s_waitcnt vmcnt(1)
	ds_write2_b64 v250, v[90:91], v[92:93] offset1:1
	s_waitcnt vmcnt(0)
	ds_write2_b64 v251, v[94:95], v[96:97] offset1:1
	v_fma_f32 v4, -v2, v3, 1.0
	v_fmac_f32_e32 v3, v4, v3
	v_div_scale_f32 v4, vcc, 1.0, v98, 1.0
	v_mul_f32_e32 v5, v4, v3
	v_fma_f32 v6, -v2, v5, v4
	v_fmac_f32_e32 v5, v6, v3
	v_fma_f32 v2, -v2, v5, v4
	v_div_fmas_f32 v2, v2, v3, v5
	v_div_fixup_f32 v50, v2, v98, 1.0
	v_mov_b32_e32 v51, v50
	s_waitcnt lgkmcnt(0)
	s_barrier
.LBB0_863:
	v_add_u32_e32 v60, s2, v219
	ds_read2_b64 v[2:5], v60 offset1:2
	ds_read2_b64 v[66:69], v60 offset0:4 offset1:6
	ds_read2_b64 v[70:73], v60 offset0:8 offset1:10
	ds_read2_b64 v[74:77], v60 offset0:12 offset1:14
	ds_read2_b64 v[78:81], v60 offset0:16 offset1:18
	ds_read2_b64 v[82:85], v60 offset0:20 offset1:22
	ds_read2_b64 v[86:89], v60 offset0:24 offset1:26
	ds_read2_b64 v[90:93], v60 offset0:28 offset1:30
	ds_read2_b64 v[94:97], v60 offset0:32 offset1:34
	ds_read2_b64 v[98:101], v60 offset0:36 offset1:38
	ds_read2_b64 v[106:109], v60 offset0:40 offset1:42
	ds_read2_b64 v[56:59], v60 offset0:44 offset1:46
	v_mov_b32_e32 v64, v1
	s_addk_i32 s2, 0x4100
	s_waitcnt lgkmcnt(11)
	v_mfma_f32_32x32x16_bf16 v[2:17], v[2:5], v[18:21], 0
	s_waitcnt lgkmcnt(10)
	v_mfma_f32_32x32x16_bf16 v[2:17], v[66:69], v[22:25], v[2:17]
	ds_read2_b64 v[66:69], v60 offset0:48 offset1:50
	s_waitcnt lgkmcnt(10)
	v_mfma_f32_32x32x16_bf16 v[2:17], v[70:73], v[26:29], v[2:17]
	ds_read2_b64 v[70:73], v60 offset0:52 offset1:54
	s_waitcnt lgkmcnt(10)
	v_mfma_f32_32x32x16_bf16 v[2:17], v[74:77], v[30:33], v[2:17]
	ds_read2_b64 v[74:77], v60 offset0:56 offset1:58
	s_waitcnt lgkmcnt(10)
	v_mfma_f32_32x32x16_bf16 v[2:17], v[78:81], v[34:37], v[2:17]
	ds_read2_b64 v[78:81], v60 offset0:60 offset1:62
	s_waitcnt lgkmcnt(10)
	v_mfma_f32_32x32x16_bf16 v[2:17], v[82:85], v[38:41], v[2:17]
	s_waitcnt lgkmcnt(9)
	v_mfma_f32_32x32x16_bf16 v[2:17], v[86:89], v[102:105], v[2:17]
	s_waitcnt lgkmcnt(8)
	v_mfma_f32_32x32x16_bf16 v[2:17], v[90:93], v[110:113], v[2:17]
	s_waitcnt lgkmcnt(7)
	v_mfma_f32_32x32x16_bf16 v[2:17], v[94:97], v[114:117], v[2:17]
	s_waitcnt lgkmcnt(6)
	v_mfma_f32_32x32x16_bf16 v[2:17], v[98:101], v[118:121], v[2:17]
	s_waitcnt lgkmcnt(5)
	v_mfma_f32_32x32x16_bf16 v[2:17], v[106:109], v[122:125], v[2:17]
	s_waitcnt lgkmcnt(4)
	v_mfma_f32_32x32x16_bf16 v[2:17], v[56:59], v[126:129], v[2:17]
	s_waitcnt lgkmcnt(3)
	v_mfma_f32_32x32x16_bf16 v[2:17], v[66:69], v[130:133], v[2:17]
	s_nop 0
	v_and_b32_e32 v142, 31, v64
	s_waitcnt lgkmcnt(2)
	v_mfma_f32_32x32x16_bf16 v[2:17], v[70:73], v[134:137], v[2:17]
	v_ashrrev_i32_e32 v52, 1, v64
	v_and_b32_e32 v52, 0xffffffe0, v52
	v_ashrrev_i32_e32 v53, 31, v52
	v_lshl_add_u64 v[52:53], s[4:5], 0, v[52:53]
	v_lshl_add_u64 v[52:53], v[52:53], 0, v[142:143]
	v_lshrrev_b32_e32 v54, 2, v64
	v_lshlrev_b64 v[52:53], 11, v[52:53]
	s_waitcnt lgkmcnt(1)
	v_mfma_f32_32x32x16_bf16 v[2:17], v[74:77], v[42:45], v[2:17]
	v_and_or_b32 v52, v54, 8, v52
	v_lshl_add_u64 v[52:53], s[6:7], 0, v[52:53]
	s_add_u32 s6, s6, 64
	s_addc_u32 s7, s7, 0
	s_cmp_lg_u32 s2, 0x20800
	s_waitcnt lgkmcnt(0)
	v_mfma_f32_32x32x16_bf16 v[2:17], v[78:81], v[46:49], v[2:17]
	s_nop 11
	v_pk_mul_f32 v[2:3], v[50:51], v[2:3]
	v_pk_mul_f32 v[4:5], v[50:51], v[4:5]
	v_pk_mul_f32 v[6:7], v[50:51], v[6:7]
	v_pk_mul_f32 v[8:9], v[50:51], v[8:9]
	v_pk_mul_f32 v[10:11], v[50:51], v[10:11]
	v_pk_mul_f32 v[12:13], v[50:51], v[12:13]
	v_pk_mul_f32 v[14:15], v[50:51], v[14:15]
	v_pk_mul_f32 v[16:17], v[50:51], v[16:17]
	v_cvt_pk_bf16_f32 v2, v2, v3
	v_cvt_pk_bf16_f32 v3, v4, v5
	v_cvt_pk_bf16_f32 v4, v6, v7
	v_cvt_pk_bf16_f32 v5, v8, v9
	v_cvt_pk_bf16_f32 v6, v10, v11
	v_cvt_pk_bf16_f32 v7, v12, v13
	v_cvt_pk_bf16_f32 v8, v14, v15
	v_cvt_pk_bf16_f32 v9, v16, v17
	global_store_dwordx2 v[52:53], v[2:3], off offset:-32
	global_store_dwordx2 v[52:53], v[4:5], off offset:-16
	global_store_dwordx2 v[52:53], v[6:7], off
	global_store_dwordx2 v[52:53], v[8:9], off offset:16
	s_cbranch_scc1 .LBB0_863
	v_readlane_b32 s4, v252, 0
	s_add_i32 s15, s15, s91
	s_add_i32 s10, s10, s11
	s_add_i32 s14, s14, s4
	s_cmpk_lt_i32 s15, 0x100
	v_readlane_b32 s5, v252, 1
	s_cbranch_scc1 .LBB0_860

.LBB0_2144:
	v_add_u32_e32 v60, s2, v219
	ds_read2_b64 v[2:5], v60 offset1:2
	ds_read2_b64 v[66:69], v60 offset0:4 offset1:6
	ds_read2_b64 v[70:73], v60 offset0:8 offset1:10
	ds_read2_b64 v[74:77], v60 offset0:12 offset1:14
	ds_read2_b64 v[78:81], v60 offset0:16 offset1:18
	ds_read2_b64 v[82:85], v60 offset0:20 offset1:22
	ds_read2_b64 v[86:89], v60 offset0:24 offset1:26
	ds_read2_b64 v[90:93], v60 offset0:28 offset1:30
	ds_read2_b64 v[94:97], v60 offset0:32 offset1:34
	ds_read2_b64 v[98:101], v60 offset0:36 offset1:38
	ds_read2_b64 v[106:109], v60 offset0:40 offset1:42
	ds_read2_b64 v[56:59], v60 offset0:44 offset1:46
	v_mov_b32_e32 v64, v1
	s_addk_i32 s2, 0x4100
	s_waitcnt lgkmcnt(11)
	v_mfma_f32_32x32x16_bf16 v[2:17], v[2:5], v[18:21], 0
	s_waitcnt lgkmcnt(10)
	v_mfma_f32_32x32x16_bf16 v[2:17], v[66:69], v[22:25], v[2:17]
	ds_read2_b64 v[66:69], v60 offset0:48 offset1:50
	s_waitcnt lgkmcnt(10)
	v_mfma_f32_32x32x16_bf16 v[2:17], v[70:73], v[26:29], v[2:17]
	ds_read2_b64 v[70:73], v60 offset0:52 offset1:54
	s_waitcnt lgkmcnt(10)
	v_mfma_f32_32x32x16_bf16 v[2:17], v[74:77], v[30:33], v[2:17]
	ds_read2_b64 v[74:77], v60 offset0:56 offset1:58
	s_waitcnt lgkmcnt(10)
	v_mfma_f32_32x32x16_bf16 v[2:17], v[78:81], v[34:37], v[2:17]
	ds_read2_b64 v[78:81], v60 offset0:60 offset1:62
	s_waitcnt lgkmcnt(10)
	v_mfma_f32_32x32x16_bf16 v[2:17], v[82:85], v[38:41], v[2:17]
	s_waitcnt lgkmcnt(9)
	v_mfma_f32_32x32x16_bf16 v[2:17], v[86:89], v[102:105], v[2:17]
	s_waitcnt lgkmcnt(8)
	v_mfma_f32_32x32x16_bf16 v[2:17], v[90:93], v[110:113], v[2:17]
	s_waitcnt lgkmcnt(7)
	v_mfma_f32_32x32x16_bf16 v[2:17], v[94:97], v[114:117], v[2:17]
	s_waitcnt lgkmcnt(6)
	v_mfma_f32_32x32x16_bf16 v[2:17], v[98:101], v[118:121], v[2:17]
	s_waitcnt lgkmcnt(5)
	v_mfma_f32_32x32x16_bf16 v[2:17], v[106:109], v[122:125], v[2:17]
	s_waitcnt lgkmcnt(4)
	v_mfma_f32_32x32x16_bf16 v[2:17], v[56:59], v[126:129], v[2:17]
	s_waitcnt lgkmcnt(3)
	v_mfma_f32_32x32x16_bf16 v[2:17], v[66:69], v[130:133], v[2:17]
	s_nop 0
	v_and_b32_e32 v142, 31, v64
	s_waitcnt lgkmcnt(2)
	v_mfma_f32_32x32x16_bf16 v[2:17], v[70:73], v[134:137], v[2:17]
	v_ashrrev_i32_e32 v52, 1, v64
	v_and_b32_e32 v52, 0xffffffe0, v52
	v_ashrrev_i32_e32 v53, 31, v52
	v_lshl_add_u64 v[52:53], s[4:5], 0, v[52:53]
	v_lshl_add_u64 v[52:53], v[52:53], 0, v[142:143]
	v_lshrrev_b32_e32 v54, 2, v64
	v_lshlrev_b64 v[52:53], 11, v[52:53]
	s_waitcnt lgkmcnt(1)
	v_mfma_f32_32x32x16_bf16 v[2:17], v[74:77], v[42:45], v[2:17]
	v_and_or_b32 v52, v54, 8, v52
	v_lshl_add_u64 v[52:53], s[6:7], 0, v[52:53]
	s_add_u32 s6, s6, 64
	s_addc_u32 s7, s7, 0
	s_cmp_lg_u32 s2, 0x20800
	s_waitcnt lgkmcnt(0)
	v_mfma_f32_32x32x16_bf16 v[2:17], v[78:81], v[46:49], v[2:17]
	s_nop 11
	v_pk_mul_f32 v[2:3], v[50:51], v[2:3]
	v_pk_mul_f32 v[4:5], v[50:51], v[4:5]
	v_pk_mul_f32 v[6:7], v[50:51], v[6:7]
	v_pk_mul_f32 v[8:9], v[50:51], v[8:9]
	v_pk_mul_f32 v[10:11], v[50:51], v[10:11]
	v_pk_mul_f32 v[12:13], v[50:51], v[12:13]
	v_pk_mul_f32 v[14:15], v[50:51], v[14:15]
	v_pk_mul_f32 v[16:17], v[50:51], v[16:17]
	v_cvt_pk_bf16_f32 v2, v2, v3
	v_cvt_pk_bf16_f32 v3, v4, v5
	v_cvt_pk_bf16_f32 v4, v6, v7
	v_cvt_pk_bf16_f32 v5, v8, v9
	v_cvt_pk_bf16_f32 v6, v10, v11
	v_cvt_pk_bf16_f32 v7, v12, v13
	v_cvt_pk_bf16_f32 v8, v14, v15
	v_cvt_pk_bf16_f32 v9, v16, v17
	global_store_dwordx2 v[52:53], v[2:3], off offset:-32
	global_store_dwordx2 v[52:53], v[4:5], off offset:-16
	global_store_dwordx2 v[52:53], v[6:7], off
	global_store_dwordx2 v[52:53], v[8:9], off offset:16
	s_cbranch_scc1 .LBB0_2144
	s_add_i32 s15, s15, s91
	s_add_i32 s10, s10, s11
	s_add_i32 s14, s14, s70
	s_cmpk_lt_i32 s15, 0x100
	s_cbranch_scc1 .LBB0_2141
